# static priority raise for waves 4-7 also in the mixer's fnet GEMM units and hyena units (per-block toggles in the fnet units removed)
# speedup vs baseline: 1.0014x; 1.0014x over previous
.LBB0_634:
	s_and_b32 s86, s6, 3
	v_and_b32_e32 v3, 15, v2
	v_and_b32_e32 v138, 48, v2
	v_lshlrev_b32_e32 v2, 2, v2
	v_lshl_add_u64 v[4:5], s[4:5], 0, v[130:131]
	v_mov_b32_e32 v135, v131
	v_lshl_or_b32 v139, s7, 6, v3
	v_lshl_or_b32 v3, v3, 6, v138
	v_and_b32_e32 v2, 32, v2
	s_lshl_b32 s6, s7, 13
	s_lshl_b32 s7, s86, 12
	v_lshl_add_u64 v[6:7], s[4:5], 0, v[134:135]
	v_bitop3_b32 v8, v3, s6, v2 bitop3:0xde
	v_bitop3_b32 v140, v3, s7, v2 bitop3:0xde
	s_add_i32 m0, s38, 0x18000
	v_lshl_add_u64 v[2:3], v[4:5], 0, s[30:31]
	v_readlane_b32 s6, v254, 34
	v_mov_b32_e32 v133, v131
	s_waitcnt vmcnt(4)
	s_barrier
	v_cmp_lt_u32_e32 vcc, 0xff, v0
	s_nop 3
	s_cbranch_vccz .Lmy_spm_fnl
	s_setprio 1
.Lmy_spm_fnl:
	global_load_lds_dwordx4 v[2:3], off
	v_lshl_add_u64 v[2:3], v[6:7], 0, s[30:31]
	s_add_i32 m0, s38, 0x1a000
	v_readlane_b32 s7, v254, 35
	s_add_i32 s87, s38, 0x8000
	v_mov_b32_e32 v137, v131
	global_load_lds_dwordx4 v[2:3], off
	v_lshl_add_u64 v[2:3], s[6:7], 0, v[132:133]
	s_mov_b32 m0, s87
	s_add_i32 s88, s38, 0xa000
	global_load_lds_dwordx4 v[2:3], off
	v_lshl_add_u64 v[2:3], s[6:7], 0, v[136:137]
	s_add_u32 s6, s4, 0x1080
	s_mov_b32 m0, s88
	s_addc_u32 s7, s5, 0
	global_load_lds_dwordx4 v[2:3], off
	s_add_i32 m0, s38, 0x1c000
	v_lshl_add_u64 v[2:3], s[6:7], 0, v[130:131]
	global_load_lds_dwordx4 v[2:3], off
	v_lshl_add_u64 v[2:3], s[6:7], 0, v[134:135]
	s_add_i32 m0, s38, 0x1e000
	v_mov_b32_e32 v10, 0
	global_load_lds_dwordx4 v[2:3], off
	s_waitcnt vmcnt(6)
	s_mov_b32 s12, 0
	s_mov_b64 s[6:7], -1
	s_mov_b64 s[10:11], 0
	v_add_u32_e32 v141, 0, v8
	v_mov_b32_e32 v11, v10
	v_mov_b32_e32 v12, v10
	v_mov_b32_e32 v13, v10
	v_mov_b32_e32 v14, v10
	v_mov_b32_e32 v15, v10
	v_mov_b32_e32 v16, v10
	v_mov_b32_e32 v17, v10
	v_mov_b32_e32 v26, v10
	v_mov_b32_e32 v27, v10
	v_mov_b32_e32 v28, v10
	v_mov_b32_e32 v29, v10
	v_mov_b32_e32 v30, v10
	v_mov_b32_e32 v31, v10
	v_mov_b32_e32 v32, v10
	v_mov_b32_e32 v33, v10
	v_mov_b32_e32 v2, v10
	v_mov_b32_e32 v3, v10
	v_mov_b32_e32 v4, v10
	v_mov_b32_e32 v5, v10
	v_mov_b32_e32 v6, v10
	v_mov_b32_e32 v7, v10
	v_mov_b32_e32 v8, v10
	v_mov_b32_e32 v9, v10
	v_mov_b32_e32 v18, v10
	v_mov_b32_e32 v19, v10
	v_mov_b32_e32 v20, v10
	v_mov_b32_e32 v21, v10
	v_mov_b32_e32 v22, v10
	v_mov_b32_e32 v23, v10
	v_mov_b32_e32 v24, v10
	v_mov_b32_e32 v25, v10
	v_mov_b32_e32 v34, v10
	v_mov_b32_e32 v35, v10
	v_mov_b32_e32 v36, v10
	v_mov_b32_e32 v37, v10
	v_mov_b32_e32 v38, v10
	v_mov_b32_e32 v39, v10
	v_mov_b32_e32 v40, v10
	v_mov_b32_e32 v41, v10
	v_mov_b32_e32 v50, v10
	v_mov_b32_e32 v51, v10
	v_mov_b32_e32 v52, v10
	v_mov_b32_e32 v53, v10
	v_mov_b32_e32 v54, v10
	v_mov_b32_e32 v55, v10
	v_mov_b32_e32 v56, v10
	v_mov_b32_e32 v57, v10
	v_mov_b32_e32 v66, v10
	v_mov_b32_e32 v67, v10
	v_mov_b32_e32 v68, v10
	v_mov_b32_e32 v69, v10
	v_mov_b32_e32 v70, v10
	v_mov_b32_e32 v71, v10
	v_mov_b32_e32 v72, v10
	v_mov_b32_e32 v73, v10
	v_mov_b32_e32 v74, v10
	v_mov_b32_e32 v75, v10
	v_mov_b32_e32 v76, v10
	v_mov_b32_e32 v77, v10
	v_mov_b32_e32 v78, v10
	v_mov_b32_e32 v79, v10
	v_mov_b32_e32 v80, v10
	v_mov_b32_e32 v81, v10
	v_mov_b32_e32 v90, v10
	v_mov_b32_e32 v91, v10
	v_mov_b32_e32 v92, v10
	v_mov_b32_e32 v93, v10
	v_mov_b32_e32 v94, v10
	v_mov_b32_e32 v95, v10
	v_mov_b32_e32 v96, v10
	v_mov_b32_e32 v97, v10
	v_mov_b32_e32 v106, v10
	v_mov_b32_e32 v107, v10
	v_mov_b32_e32 v108, v10
	v_mov_b32_e32 v109, v10
	v_mov_b32_e32 v110, v10
	v_mov_b32_e32 v111, v10
	v_mov_b32_e32 v112, v10
	v_mov_b32_e32 v113, v10
	v_mov_b32_e32 v82, v10
	v_mov_b32_e32 v83, v10
	v_mov_b32_e32 v84, v10
	v_mov_b32_e32 v85, v10
	v_mov_b32_e32 v86, v10
	v_mov_b32_e32 v87, v10
	v_mov_b32_e32 v88, v10
	v_mov_b32_e32 v89, v10
	v_mov_b32_e32 v98, v10
	v_mov_b32_e32 v99, v10
	v_mov_b32_e32 v100, v10
	v_mov_b32_e32 v101, v10
	v_mov_b32_e32 v102, v10
	v_mov_b32_e32 v103, v10
	v_mov_b32_e32 v104, v10
	v_mov_b32_e32 v105, v10
	v_mov_b32_e32 v114, v10
	v_mov_b32_e32 v115, v10
	v_mov_b32_e32 v116, v10
	v_mov_b32_e32 v117, v10
	v_mov_b32_e32 v118, v10
	v_mov_b32_e32 v119, v10
	v_mov_b32_e32 v120, v10
	v_mov_b32_e32 v121, v10
	v_mov_b32_e32 v122, v10
	v_mov_b32_e32 v123, v10
	v_mov_b32_e32 v124, v10
	v_mov_b32_e32 v125, v10
	v_mov_b32_e32 v126, v10
	v_mov_b32_e32 v127, v10
	v_mov_b32_e32 v128, v10
	v_mov_b32_e32 v129, v10
	v_mov_b32_e32 v58, v10
	v_mov_b32_e32 v59, v10
	v_mov_b32_e32 v60, v10
	v_mov_b32_e32 v61, v10
	v_mov_b32_e32 v62, v10
	v_mov_b32_e32 v63, v10
	v_mov_b32_e32 v64, v10
	v_mov_b32_e32 v65, v10
	v_mov_b32_e32 v42, v10
	v_mov_b32_e32 v43, v10
	v_mov_b32_e32 v44, v10
	v_mov_b32_e32 v45, v10
	v_mov_b32_e32 v46, v10
	v_mov_b32_e32 v47, v10
	v_mov_b32_e32 v48, v10
	v_mov_b32_e32 v49, v10
	s_barrier
.LBB0_635:
	s_add_i32 s13, s12, 0x100
	s_and_b64 s[10:11], s[10:11], exec
	s_cselect_b32 s11, 0, s13
	s_cselect_b32 s10, 0, 0
	s_add_u32 s16, s74, s11
	s_addc_u32 s17, s75, s10
	s_add_u32 s18, s4, s11
	s_addc_u32 s19, s5, s10
	s_add_i32 s11, 0, 0x10000
	s_add_u32 s84, s76, s12
	s_addc_u32 s85, s77, 0
	s_add_i32 s43, s11, s33
	s_add_i32 m0, s38, 0xc000
	s_add_i32 s60, s38, 0xe000
	s_add_i32 s94, 0, 0x14000
	s_add_i32 s27, s43, 0x2000
	s_add_u32 s14, s18, 0x1000
	v_add_u32_e32 v154, s11, v140
	s_addc_u32 s15, s19, 0
	s_add_i32 s93, s94, s33
	ds_read_b128 v[142:145], v154
	ds_read_b128 v[146:149], v154 offset:1024
	ds_read_b128 v[150:153], v154 offset:2048
	ds_read_b128 v[154:157], v154 offset:3072
	s_add_i32 s96, s93, 0x2000
	s_add_i32 s92, 0, 0x18000
	s_add_u32 s12, s16, 0x10000
	s_addc_u32 s13, s17, 0
	s_add_i32 s91, s92, s33
	s_add_i32 s90, 0, 0x1c000
	s_add_i32 s89, s91, 0x2000
	s_add_u32 s10, s18, 0x1080
	s_addc_u32 s11, s19, 0
	s_add_i32 vcc_hi, s90, s33
	s_add_i32 vcc_lo, vcc_hi, 0x2000
	v_lshl_add_u64 v[174:175], s[84:85], 0, v[132:133]
	v_lshl_add_u64 v[174:175], v[174:175], 0, s[30:31]
	ds_read_b128 v[158:161], v141
	ds_read_b128 v[162:165], v141 offset:1024
	ds_read_b128 v[166:169], v141 offset:2048
	ds_read_b128 v[170:173], v141 offset:3072
	ds_read_b128 v[178:181], v141 offset:4096
	ds_read_b128 v[182:185], v141 offset:5120
	ds_read_b128 v[188:191], v141 offset:6144
	ds_read_b128 v[192:195], v141 offset:7168
	global_load_lds_dwordx4 v[174:175], off
	v_lshl_add_u64 v[174:175], s[84:85], 0, v[136:137]
	v_lshl_add_u64 v[174:175], v[174:175], 0, s[30:31]
	s_mov_b32 m0, s60
	s_nop 0
	global_load_lds_dwordx4 v[174:175], off
	s_waitcnt lgkmcnt(8)
	s_waitcnt vmcnt(10)
	s_barrier
	s_waitcnt lgkmcnt(7)
	v_mfma_f32_16x16x32_bf16 v[126:129], v[142:145], v[158:161], v[126:129]
	s_waitcnt lgkmcnt(5)
	v_mfma_f32_16x16x32_bf16 v[122:125], v[150:153], v[158:161], v[122:125]
	v_mfma_f32_16x16x32_bf16 v[118:121], v[142:145], v[166:169], v[118:121]
	s_waitcnt lgkmcnt(3)
	v_mfma_f32_16x16x32_bf16 v[114:117], v[150:153], v[166:169], v[114:117]
	v_mfma_f32_16x16x32_bf16 v[102:105], v[142:145], v[178:181], v[102:105]
	s_waitcnt lgkmcnt(1)
	v_mfma_f32_16x16x32_bf16 v[98:101], v[150:153], v[178:181], v[98:101]
	v_mfma_f32_16x16x32_bf16 v[86:89], v[142:145], v[188:191], v[86:89]
	v_mfma_f32_16x16x32_bf16 v[82:85], v[150:153], v[188:191], v[82:85]
	v_mfma_f32_16x16x32_bf16 v[126:129], v[146:149], v[162:165], v[126:129]
	v_mfma_f32_16x16x32_bf16 v[122:125], v[154:157], v[162:165], v[122:125]
	v_mfma_f32_16x16x32_bf16 v[118:121], v[146:149], v[170:173], v[118:121]
	v_mfma_f32_16x16x32_bf16 v[114:117], v[154:157], v[170:173], v[114:117]
	v_mfma_f32_16x16x32_bf16 v[102:105], v[146:149], v[182:185], v[102:105]
	s_waitcnt lgkmcnt(0)
	v_mfma_f32_16x16x32_bf16 v[98:101], v[154:157], v[182:185], v[98:101]
	v_mfma_f32_16x16x32_bf16 v[86:89], v[146:149], v[192:195], v[86:89]
	v_mfma_f32_16x16x32_bf16 v[82:85], v[154:157], v[192:195], v[82:85]
	s_barrier
	v_add_u32_e32 v174, s94, v140
	s_mov_b32 m0, s43
	ds_read_b128 v[196:199], v174
	ds_read_b128 v[218:221], v174 offset:1024
	ds_read_b128 v[222:225], v174 offset:2048
	ds_read_b128 v[226:229], v174 offset:3072
	v_lshl_add_u64 v[174:175], s[18:19], 0, v[130:131]
	global_load_lds_dwordx4 v[174:175], off
	v_lshl_add_u64 v[200:201], s[18:19], 0, v[134:135]
	s_mov_b32 m0, s27
	s_nop 0
	global_load_lds_dwordx4 v[200:201], off
	s_waitcnt vmcnt(10)
	s_barrier
	s_waitcnt lgkmcnt(3)
	s_waitcnt lgkmcnt(1)
	v_mfma_f32_16x16x32_bf16 v[110:113], v[196:199], v[158:161], v[110:113]
	v_mfma_f32_16x16x32_bf16 v[106:109], v[222:225], v[158:161], v[106:109]
	v_mfma_f32_16x16x32_bf16 v[94:97], v[196:199], v[166:169], v[94:97]
	v_mfma_f32_16x16x32_bf16 v[90:93], v[222:225], v[166:169], v[90:93]
	v_mfma_f32_16x16x32_bf16 v[78:81], v[196:199], v[178:181], v[78:81]
	v_mfma_f32_16x16x32_bf16 v[74:77], v[222:225], v[178:181], v[74:77]
	v_mfma_f32_16x16x32_bf16 v[70:73], v[196:199], v[188:191], v[70:73]
	v_mfma_f32_16x16x32_bf16 v[66:69], v[222:225], v[188:191], v[66:69]
	s_waitcnt lgkmcnt(0)
	v_mfma_f32_16x16x32_bf16 v[110:113], v[218:221], v[162:165], v[110:113]
	v_mfma_f32_16x16x32_bf16 v[106:109], v[226:229], v[162:165], v[106:109]
	v_mfma_f32_16x16x32_bf16 v[94:97], v[218:221], v[170:173], v[94:97]
	v_mfma_f32_16x16x32_bf16 v[90:93], v[226:229], v[170:173], v[90:93]
	v_mfma_f32_16x16x32_bf16 v[78:81], v[218:221], v[182:185], v[78:81]
	v_mfma_f32_16x16x32_bf16 v[74:77], v[226:229], v[182:185], v[74:77]
	v_mfma_f32_16x16x32_bf16 v[70:73], v[218:221], v[192:195], v[70:73]
	v_mfma_f32_16x16x32_bf16 v[66:69], v[226:229], v[192:195], v[66:69]
	s_mov_b32 m0, s38
	v_lshl_add_u64 v[230:231], s[16:17], 0, v[132:133]
	s_barrier
	ds_read_b128 v[158:161], v141 offset:16384
	ds_read_b128 v[162:165], v141 offset:17408
	ds_read_b128 v[166:169], v141 offset:18432
	ds_read_b128 v[170:173], v141 offset:19456
	ds_read_b128 v[178:181], v141 offset:20480
	ds_read_b128 v[182:185], v141 offset:21504
	ds_read_b128 v[188:191], v141 offset:22528
	ds_read_b128 v[192:195], v141 offset:23552
	global_load_lds_dwordx4 v[230:231], off
	v_lshl_add_u64 v[232:233], s[16:17], 0, v[136:137]
	s_mov_b32 m0, s39
	s_nop 0
	global_load_lds_dwordx4 v[232:233], off
	s_barrier
	s_waitcnt lgkmcnt(7)
	v_mfma_f32_16x16x32_bf16 v[54:57], v[142:145], v[158:161], v[54:57]
	s_waitcnt lgkmcnt(5)
	v_mfma_f32_16x16x32_bf16 v[50:53], v[150:153], v[158:161], v[50:53]
	v_mfma_f32_16x16x32_bf16 v[38:41], v[142:145], v[166:169], v[38:41]
	s_waitcnt lgkmcnt(3)
	v_mfma_f32_16x16x32_bf16 v[34:37], v[150:153], v[166:169], v[34:37]
	v_mfma_f32_16x16x32_bf16 v[22:25], v[142:145], v[178:181], v[22:25]
	s_waitcnt lgkmcnt(1)
	v_mfma_f32_16x16x32_bf16 v[18:21], v[150:153], v[178:181], v[18:21]
	v_mfma_f32_16x16x32_bf16 v[6:9], v[142:145], v[188:191], v[6:9]
	v_mfma_f32_16x16x32_bf16 v[2:5], v[150:153], v[188:191], v[2:5]
	v_mfma_f32_16x16x32_bf16 v[54:57], v[146:149], v[162:165], v[54:57]
	v_mfma_f32_16x16x32_bf16 v[50:53], v[154:157], v[162:165], v[50:53]
	v_mfma_f32_16x16x32_bf16 v[38:41], v[146:149], v[170:173], v[38:41]
	v_mfma_f32_16x16x32_bf16 v[34:37], v[154:157], v[170:173], v[34:37]
	v_mfma_f32_16x16x32_bf16 v[22:25], v[146:149], v[182:185], v[22:25]
	s_waitcnt lgkmcnt(0)
	v_mfma_f32_16x16x32_bf16 v[18:21], v[154:157], v[182:185], v[18:21]
	v_mfma_f32_16x16x32_bf16 v[6:9], v[146:149], v[192:195], v[6:9]
	v_mfma_f32_16x16x32_bf16 v[2:5], v[154:157], v[192:195], v[2:5]
	s_barrier
	s_mov_b32 m0, s93
	v_lshl_add_u64 v[142:143], s[14:15], 0, v[130:131]
	global_load_lds_dwordx4 v[142:143], off
	v_lshl_add_u64 v[142:143], s[14:15], 0, v[134:135]
	s_mov_b32 m0, s96
	s_nop 0
	global_load_lds_dwordx4 v[142:143], off
	s_waitcnt vmcnt(10)
	s_barrier
	v_mfma_f32_16x16x32_bf16 v[30:33], v[196:199], v[158:161], v[30:33]
	v_mfma_f32_16x16x32_bf16 v[26:29], v[222:225], v[158:161], v[26:29]
	v_mfma_f32_16x16x32_bf16 v[14:17], v[196:199], v[166:169], v[14:17]
	v_mfma_f32_16x16x32_bf16 v[10:13], v[222:225], v[166:169], v[10:13]
	v_mfma_f32_16x16x32_bf16 v[58:61], v[196:199], v[178:181], v[58:61]
	v_mfma_f32_16x16x32_bf16 v[62:65], v[222:225], v[178:181], v[62:65]
	v_mfma_f32_16x16x32_bf16 v[42:45], v[196:199], v[188:191], v[42:45]
	v_mfma_f32_16x16x32_bf16 v[46:49], v[222:225], v[188:191], v[46:49]
	v_mfma_f32_16x16x32_bf16 v[30:33], v[218:221], v[162:165], v[30:33]
	v_mfma_f32_16x16x32_bf16 v[26:29], v[226:229], v[162:165], v[26:29]
	v_mfma_f32_16x16x32_bf16 v[14:17], v[218:221], v[170:173], v[14:17]
	v_mfma_f32_16x16x32_bf16 v[10:13], v[226:229], v[170:173], v[10:13]
	v_mfma_f32_16x16x32_bf16 v[58:61], v[218:221], v[182:185], v[58:61]
	v_mfma_f32_16x16x32_bf16 v[62:65], v[226:229], v[182:185], v[62:65]
	v_mfma_f32_16x16x32_bf16 v[42:45], v[218:221], v[192:195], v[42:45]
	v_mfma_f32_16x16x32_bf16 v[46:49], v[226:229], v[192:195], v[46:49]
	v_add_u32_e32 v154, s92, v140
	s_barrier
	ds_read_b128 v[142:145], v154
	ds_read_b128 v[146:149], v154 offset:1024
	ds_read_b128 v[150:153], v154 offset:2048
	ds_read_b128 v[154:157], v154 offset:3072
	s_mov_b32 m0, s42
	v_lshl_add_u64 v[196:197], s[12:13], 0, v[132:133]
	ds_read_b128 v[158:161], v141 offset:32768
	ds_read_b128 v[162:165], v141 offset:33792
	ds_read_b128 v[166:169], v141 offset:34816
	ds_read_b128 v[170:173], v141 offset:35840
	ds_read_b128 v[178:181], v141 offset:36864
	ds_read_b128 v[182:185], v141 offset:37888
	ds_read_b128 v[188:191], v141 offset:38912
	ds_read_b128 v[192:195], v141 offset:39936
	global_load_lds_dwordx4 v[196:197], off
	v_lshl_add_u64 v[196:197], s[12:13], 0, v[136:137]
	s_mov_b32 m0, s64
	s_nop 0
	global_load_lds_dwordx4 v[196:197], off
	s_waitcnt lgkmcnt(8)
	s_waitcnt vmcnt(10)
	s_barrier
	s_waitcnt lgkmcnt(7)
	v_mfma_f32_16x16x32_bf16 v[126:129], v[142:145], v[158:161], v[126:129]
	s_waitcnt lgkmcnt(5)
	v_mfma_f32_16x16x32_bf16 v[122:125], v[150:153], v[158:161], v[122:125]
	v_mfma_f32_16x16x32_bf16 v[118:121], v[142:145], v[166:169], v[118:121]
	s_waitcnt lgkmcnt(3)
	v_mfma_f32_16x16x32_bf16 v[114:117], v[150:153], v[166:169], v[114:117]
	v_mfma_f32_16x16x32_bf16 v[102:105], v[142:145], v[178:181], v[102:105]
	s_waitcnt lgkmcnt(1)
	v_mfma_f32_16x16x32_bf16 v[98:101], v[150:153], v[178:181], v[98:101]
	v_mfma_f32_16x16x32_bf16 v[86:89], v[142:145], v[188:191], v[86:89]
	v_mfma_f32_16x16x32_bf16 v[82:85], v[150:153], v[188:191], v[82:85]
	v_mfma_f32_16x16x32_bf16 v[126:129], v[146:149], v[162:165], v[126:129]
	v_mfma_f32_16x16x32_bf16 v[122:125], v[154:157], v[162:165], v[122:125]
	v_mfma_f32_16x16x32_bf16 v[118:121], v[146:149], v[170:173], v[118:121]
	v_mfma_f32_16x16x32_bf16 v[114:117], v[154:157], v[170:173], v[114:117]
	v_mfma_f32_16x16x32_bf16 v[102:105], v[146:149], v[182:185], v[102:105]
	s_waitcnt lgkmcnt(0)
	v_mfma_f32_16x16x32_bf16 v[98:101], v[154:157], v[182:185], v[98:101]
	v_mfma_f32_16x16x32_bf16 v[86:89], v[146:149], v[192:195], v[86:89]
	v_mfma_f32_16x16x32_bf16 v[82:85], v[154:157], v[192:195], v[82:85]
	s_barrier
	s_mov_b32 m0, s91
	v_add_u32_e32 v187, s90, v140
	v_lshl_add_u64 v[174:175], v[174:175], 0, s[30:31]
	ds_read_b128 v[196:199], v187
	ds_read_b128 v[218:221], v187 offset:1024
	ds_read_b128 v[222:225], v187 offset:2048
	ds_read_b128 v[226:229], v187 offset:3072
	global_load_lds_dwordx4 v[174:175], off
	v_lshl_add_u64 v[174:175], v[200:201], 0, s[30:31]
	s_mov_b32 m0, s89
	s_nop 0
	global_load_lds_dwordx4 v[174:175], off
	s_waitcnt vmcnt(10)
	s_barrier
	s_waitcnt lgkmcnt(3)
	s_waitcnt lgkmcnt(1)
	v_mfma_f32_16x16x32_bf16 v[110:113], v[196:199], v[158:161], v[110:113]
	v_mfma_f32_16x16x32_bf16 v[106:109], v[222:225], v[158:161], v[106:109]
	v_mfma_f32_16x16x32_bf16 v[94:97], v[196:199], v[166:169], v[94:97]
	v_mfma_f32_16x16x32_bf16 v[90:93], v[222:225], v[166:169], v[90:93]
	v_mfma_f32_16x16x32_bf16 v[78:81], v[196:199], v[178:181], v[78:81]
	v_mfma_f32_16x16x32_bf16 v[74:77], v[222:225], v[178:181], v[74:77]
	v_mfma_f32_16x16x32_bf16 v[70:73], v[196:199], v[188:191], v[70:73]
	v_mfma_f32_16x16x32_bf16 v[66:69], v[222:225], v[188:191], v[66:69]
	s_waitcnt lgkmcnt(0)
	v_mfma_f32_16x16x32_bf16 v[110:113], v[218:221], v[162:165], v[110:113]
	v_mfma_f32_16x16x32_bf16 v[106:109], v[226:229], v[162:165], v[106:109]
	v_mfma_f32_16x16x32_bf16 v[94:97], v[218:221], v[170:173], v[94:97]
	v_mfma_f32_16x16x32_bf16 v[90:93], v[226:229], v[170:173], v[90:93]
	v_mfma_f32_16x16x32_bf16 v[78:81], v[218:221], v[182:185], v[78:81]
	v_mfma_f32_16x16x32_bf16 v[74:77], v[226:229], v[182:185], v[74:77]
	v_mfma_f32_16x16x32_bf16 v[70:73], v[218:221], v[192:195], v[70:73]
	v_mfma_f32_16x16x32_bf16 v[66:69], v[226:229], v[192:195], v[66:69]
	s_mov_b32 m0, s87
	v_lshl_add_u64 v[174:175], v[230:231], 0, s[30:31]
	s_barrier
	ds_read_b128 v[158:161], v141 offset:49152
	ds_read_b128 v[162:165], v141 offset:50176
	ds_read_b128 v[166:169], v141 offset:51200
	ds_read_b128 v[170:173], v141 offset:52224
	ds_read_b128 v[178:181], v141 offset:53248
	ds_read_b128 v[182:185], v141 offset:54272
	ds_read_b128 v[188:191], v141 offset:55296
	ds_read_b128 v[192:195], v141 offset:56320
	global_load_lds_dwordx4 v[174:175], off
	v_lshl_add_u64 v[174:175], v[232:233], 0, s[30:31]
	s_mov_b32 m0, s88
	s_nop 0
	global_load_lds_dwordx4 v[174:175], off
	s_barrier
	s_waitcnt lgkmcnt(7)
	v_mfma_f32_16x16x32_bf16 v[54:57], v[142:145], v[158:161], v[54:57]
	s_waitcnt lgkmcnt(5)
	v_mfma_f32_16x16x32_bf16 v[50:53], v[150:153], v[158:161], v[50:53]
	v_mfma_f32_16x16x32_bf16 v[38:41], v[142:145], v[166:169], v[38:41]
	s_waitcnt lgkmcnt(3)
	v_mfma_f32_16x16x32_bf16 v[34:37], v[150:153], v[166:169], v[34:37]
	v_mfma_f32_16x16x32_bf16 v[22:25], v[142:145], v[178:181], v[22:25]
	s_waitcnt lgkmcnt(1)
	v_mfma_f32_16x16x32_bf16 v[18:21], v[150:153], v[178:181], v[18:21]
	v_mfma_f32_16x16x32_bf16 v[6:9], v[142:145], v[188:191], v[6:9]
	v_mfma_f32_16x16x32_bf16 v[2:5], v[150:153], v[188:191], v[2:5]
	v_mfma_f32_16x16x32_bf16 v[54:57], v[146:149], v[162:165], v[54:57]
	v_mfma_f32_16x16x32_bf16 v[50:53], v[154:157], v[162:165], v[50:53]
	v_mfma_f32_16x16x32_bf16 v[38:41], v[146:149], v[170:173], v[38:41]
	v_mfma_f32_16x16x32_bf16 v[34:37], v[154:157], v[170:173], v[34:37]
	v_mfma_f32_16x16x32_bf16 v[22:25], v[146:149], v[182:185], v[22:25]
	s_waitcnt lgkmcnt(0)
	v_mfma_f32_16x16x32_bf16 v[18:21], v[154:157], v[182:185], v[18:21]
	v_mfma_f32_16x16x32_bf16 v[6:9], v[146:149], v[192:195], v[6:9]
	v_mfma_f32_16x16x32_bf16 v[2:5], v[154:157], v[192:195], v[2:5]
	s_barrier
	s_mov_b32 m0, vcc_hi
	v_lshl_add_u64 v[142:143], s[10:11], 0, v[130:131]
	global_load_lds_dwordx4 v[142:143], off
	v_lshl_add_u64 v[142:143], s[10:11], 0, v[134:135]
	s_mov_b32 m0, vcc_lo
	s_nop 0
	global_load_lds_dwordx4 v[142:143], off
	s_waitcnt vmcnt(10)
	s_barrier
	v_mfma_f32_16x16x32_bf16 v[30:33], v[196:199], v[158:161], v[30:33]
	v_mfma_f32_16x16x32_bf16 v[26:29], v[222:225], v[158:161], v[26:29]
	v_mfma_f32_16x16x32_bf16 v[14:17], v[196:199], v[166:169], v[14:17]
	v_mfma_f32_16x16x32_bf16 v[10:13], v[222:225], v[166:169], v[10:13]
	v_mfma_f32_16x16x32_bf16 v[58:61], v[196:199], v[178:181], v[58:61]
	v_mfma_f32_16x16x32_bf16 v[62:65], v[222:225], v[178:181], v[62:65]
	v_mfma_f32_16x16x32_bf16 v[42:45], v[196:199], v[188:191], v[42:45]
	v_mfma_f32_16x16x32_bf16 v[46:49], v[222:225], v[188:191], v[46:49]
	v_mfma_f32_16x16x32_bf16 v[30:33], v[218:221], v[162:165], v[30:33]
	v_mfma_f32_16x16x32_bf16 v[26:29], v[226:229], v[162:165], v[26:29]
	v_mfma_f32_16x16x32_bf16 v[14:17], v[218:221], v[170:173], v[14:17]
	v_mfma_f32_16x16x32_bf16 v[10:13], v[226:229], v[170:173], v[10:13]
	v_mfma_f32_16x16x32_bf16 v[58:61], v[218:221], v[182:185], v[58:61]
	v_mfma_f32_16x16x32_bf16 v[62:65], v[226:229], v[182:185], v[62:65]
	v_mfma_f32_16x16x32_bf16 v[42:45], v[218:221], v[192:195], v[42:45]
	v_mfma_f32_16x16x32_bf16 v[46:49], v[226:229], v[192:195], v[46:49]
	s_andn2_b64 vcc, exec, s[6:7]
	s_mov_b64 s[10:11], -1
	s_mov_b64 s[6:7], 0
	s_movk_i32 s12, 0x100
	s_barrier
	s_cbranch_vccz .LBB0_635
	s_mul_i32 s4, s22, 0x900
	s_add_i32 s22, s4, 0x800
	s_lshl_b32 s6, s86, 6
	s_lshl_b64 s[4:5], s[22:23], 11
	s_add_u32 s4, s68, s4
	v_lshlrev_b32_e32 v130, 10, v139
	s_addc_u32 s5, s69, s5
	v_or3_b32 v130, v130, s6, v138
	v_cvt_pk_bf16_f32 v126, v126, v127
	v_lshl_add_u64 v[132:133], v[130:131], 1, s[4:5]
	s_mov_b64 s[4:5], 0x5ed68600
	v_lshl_add_u64 v[134:135], v[132:133], 0, s[4:5]
	s_mov_b32 s4, 0x5ed68000
	v_cvt_pk_bf16_f32 v127, v128, v129
	v_cvt_pk_bf16_f32 v128, v122, v123
	v_add_co_u32_e32 v122, vcc, s4, v132
	v_cvt_pk_bf16_f32 v110, v110, v111
	s_nop 0
	v_addc_co_u32_e32 v123, vcc, 0, v133, vcc
	v_cvt_pk_bf16_f32 v111, v112, v113
	v_cvt_pk_bf16_f32 v112, v106, v107
	v_cvt_pk_bf16_f32 v113, v108, v109
	s_mov_b32 s4, 0x5ed70000
	global_store_dwordx4 v[134:135], v[110:113], off offset:16
	v_cvt_pk_bf16_f32 v94, v94, v95
	v_cvt_pk_bf16_f32 v95, v96, v97
	v_add_co_u32_e32 v110, vcc, s4, v132
	v_cvt_pk_bf16_f32 v96, v90, v91
	s_nop 0
	v_addc_co_u32_e32 v111, vcc, 0, v133, vcc
	v_cvt_pk_bf16_f32 v97, v92, v93
	s_mov_b32 s4, 0x5ed78000
	global_store_dwordx4 v[110:111], v[94:97], off offset:1552
	v_cvt_pk_bf16_f32 v78, v78, v79
	v_cvt_pk_bf16_f32 v79, v80, v81
	v_add_co_u32_e32 v94, vcc, s4, v132
	v_cvt_pk_bf16_f32 v80, v74, v75
	s_nop 0
	v_addc_co_u32_e32 v95, vcc, 0, v133, vcc
	v_cvt_pk_bf16_f32 v81, v76, v77
	s_mov_b32 s4, 0x5ed80000
	global_store_dwordx4 v[94:95], v[78:81], off offset:1552
	v_cvt_pk_bf16_f32 v54, v54, v55
	v_cvt_pk_bf16_f32 v55, v56, v57
	v_add_co_u32_e32 v78, vcc, s4, v132
	s_mov_b32 s4, 0x5eda8000
	s_nop 0
	v_addc_co_u32_e32 v79, vcc, 0, v133, vcc
	v_cvt_pk_bf16_f32 v56, v50, v51
	v_add_co_u32_e32 v50, vcc, s4, v132
	v_cvt_pk_bf16_f32 v30, v30, v31
	s_nop 0
	v_addc_co_u32_e32 v51, vcc, 0, v133, vcc
	v_cvt_pk_bf16_f32 v31, v32, v33
	v_cvt_pk_bf16_f32 v32, v26, v27
	v_cvt_pk_bf16_f32 v33, v28, v29
	s_mov_b32 s4, 0x5edb0000
	global_store_dwordx4 v[50:51], v[30:33], off offset:1552
	v_cvt_pk_bf16_f32 v14, v14, v15
	v_cvt_pk_bf16_f32 v15, v16, v17
	v_add_co_u32_e32 v30, vcc, s4, v132
	v_cvt_pk_bf16_f32 v16, v10, v11
	s_nop 0
	v_addc_co_u32_e32 v31, vcc, 0, v133, vcc
	v_cvt_pk_bf16_f32 v17, v12, v13
	s_mov_b32 s4, 0x5edb8000
	global_store_dwordx4 v[30:31], v[14:17], off offset:1552
	v_cvt_pk_bf16_f32 v10, v22, v23
	v_cvt_pk_bf16_f32 v11, v24, v25
	v_add_co_u32_e32 v14, vcc, s4, v132
	v_cvt_pk_bf16_f32 v12, v18, v19
	v_cvt_pk_bf16_f32 v13, v20, v21
	v_addc_co_u32_e32 v15, vcc, 0, v133, vcc
	global_store_dwordx4 v[14:15], v[10:13], off offset:1536
	s_mov_b32 s4, 0x5edc0000
	v_cvt_pk_bf16_f32 v129, v124, v125
	v_cvt_pk_bf16_f32 v10, v58, v59
	v_cvt_pk_bf16_f32 v11, v60, v61
	v_cvt_pk_bf16_f32 v12, v62, v63
	v_cvt_pk_bf16_f32 v13, v64, v65
	global_store_dwordx4 v[14:15], v[10:13], off offset:1552
	v_cvt_pk_bf16_f32 v106, v118, v119
	v_cvt_pk_bf16_f32 v107, v120, v121
	v_add_co_u32_e32 v10, vcc, s4, v132
	v_cvt_pk_bf16_f32 v108, v114, v115
	v_cvt_pk_bf16_f32 v109, v116, v117
	v_cvt_pk_bf16_f32 v90, v102, v103
	v_cvt_pk_bf16_f32 v91, v104, v105
	v_cvt_pk_bf16_f32 v92, v98, v99
	v_cvt_pk_bf16_f32 v93, v100, v101
	v_cvt_pk_bf16_f32 v74, v86, v87
	v_cvt_pk_bf16_f32 v75, v88, v89
	v_cvt_pk_bf16_f32 v76, v82, v83
	v_cvt_pk_bf16_f32 v77, v84, v85
	v_cvt_pk_bf16_f32 v70, v70, v71
	v_cvt_pk_bf16_f32 v71, v72, v73
	v_cvt_pk_bf16_f32 v72, v66, v67
	v_cvt_pk_bf16_f32 v73, v68, v69
	v_cvt_pk_bf16_f32 v57, v52, v53
	v_cvt_pk_bf16_f32 v26, v38, v39
	v_cvt_pk_bf16_f32 v27, v40, v41
	v_cvt_pk_bf16_f32 v28, v34, v35
	v_cvt_pk_bf16_f32 v29, v36, v37
	v_cvt_pk_bf16_f32 v6, v6, v7
	v_cvt_pk_bf16_f32 v7, v8, v9
	v_cvt_pk_bf16_f32 v8, v2, v3
	v_cvt_pk_bf16_f32 v9, v4, v5
	v_addc_co_u32_e32 v11, vcc, 0, v133, vcc
	v_cvt_pk_bf16_f32 v2, v42, v43
	v_cvt_pk_bf16_f32 v3, v44, v45
	v_cvt_pk_bf16_f32 v4, v46, v47
	v_cvt_pk_bf16_f32 v5, v48, v49
	global_store_dwordx4 v[122:123], v[126:129], off offset:1536
	global_store_dwordx4 v[110:111], v[106:109], off offset:1536
	global_store_dwordx4 v[94:95], v[90:93], off offset:1536
	global_store_dwordx4 v[78:79], v[74:77], off offset:1536
	global_store_dwordx4 v[78:79], v[70:73], off offset:1552
	global_store_dwordx4 v[50:51], v[54:57], off offset:1536
	global_store_dwordx4 v[30:31], v[26:29], off offset:1536
	global_store_dwordx4 v[10:11], v[6:9], off offset:1536
	global_store_dwordx4 v[10:11], v[2:5], off offset:1552
	s_waitcnt vmcnt(0)
	s_setprio 0
	s_cmpk_lt_u32 s1, 0x100
	s_cbranch_scc0 .LBB0_638
	s_barrier

.LBB0_646:
	v_mov_b32_e32 v2, v0
	s_load_dwordx4 s[4:7], s[66:67], 0x58
	v_readlane_b32 s1, v254, 46
	s_add_i32 s10, s1, s57
	v_readlane_b32 s1, v254, 10
	s_mov_b32 s11, s23
	s_waitcnt lgkmcnt(0)
	s_add_u32 s1, s4, s1
	v_readlane_b32 s4, v254, 12
	s_addc_u32 s18, s5, s4
	v_readlane_b32 s4, v254, 5
	s_add_u32 s19, s6, s4
	v_readlane_b32 s4, v254, 14
	s_addc_u32 s33, s7, s4
	s_movk_i32 s4, 0x200
	v_cmp_gt_i32_e32 vcc, s4, v2
	v_ashrrev_i32_e32 v6, 1, v2
	v_lshlrev_b32_e32 v7, 4, v2
	s_waitcnt vmcnt(0)
	s_barrier
	v_readfirstlane_b32 s42, v0
	s_nop 3
	s_cmp_lt_u32 s42, 0x100
	s_cbranch_scc1 .Lmy_spm_hc
	s_setprio 1
.Lmy_spm_hc:
	s_and_saveexec_b64 s[4:5], vcc
	s_cbranch_execz .LBB0_648
	v_lshlrev_b32_e32 v4, 8, v2
	s_lshl_b64 s[6:7], s[10:11], 13
	v_and_b32_e32 v4, 0xf00, v4
	v_and_b32_e32 v5, -8, v6
	s_add_u32 s6, s50, s6
	v_add_u32_e32 v4, v4, v5
	s_addc_u32 s7, s51, s7
	v_ashrrev_i32_e32 v5, 31, v4
	v_lshl_add_u64 v[12:13], v[4:5], 1, s[6:7]
	global_load_dwordx4 v[8:11], v[12:13], off
	global_load_ushort v5, v[12:13], off offset:16
	s_movk_i32 s6, 0x1ef
	global_load_ushort v12, v[12:13], off offset:-2
	v_cmp_lt_i32_e32 vcc, s6, v2
	s_lshl_b64 s[6:7], s[10:11], 2
	s_add_u32 s12, s19, s6
	s_addc_u32 s13, s33, s7
	v_cndmask_b32_e64 v4, 1.0, 0, vcc
	v_cmp_lt_i32_e32 vcc, 15, v2
	s_add_u32 s6, s1, s6
	s_addc_u32 s7, s18, s7
	v_add_u32_e32 v3, 0, v7
	s_waitcnt vmcnt(2)
	v_lshlrev_b32_e32 v17, 16, v8
	s_waitcnt vmcnt(1)
	v_lshlrev_b32_e32 v5, 16, v5
	v_mul_f32_e32 v5, v4, v5
	v_cndmask_b32_e64 v4, 0, 1.0, vcc
	s_waitcnt vmcnt(0)
	v_lshlrev_b32_e32 v12, 16, v12
	v_mul_f32_e32 v16, v4, v12
	global_load_dword v4, v131, s[12:13]
	global_load_dword v12, v1, s[6:7] offset:2048
	global_load_dword v18, v131, s[6:7] offset:3072
	global_load_dword v20, v131, s[6:7]
	v_and_b32_e32 v8, 0xffff0000, v8
	v_and_b32_e32 v25, 16, v10
	v_and_b32_e32 v24, 0xffff0000, v9
	v_lshlrev_b32_e32 v9, 16, v9
	v_lshlrev_b32_e32 v22, 16, v11
	v_and_b32_e32 v14, 0xffff0000, v10
	v_and_b32_e32 v23, 0xffff0000, v11
	v_mov_b32_e32 v15, v22
	v_lshlrev_b32_e32 v11, 16, v10
	v_mov_b32_e32 v10, v24
	s_waitcnt vmcnt(0)
	v_pk_fma_f32 v[26:27], v[20:21], v[16:17], v[4:5] op_sel_hi:[0,1,0]
	v_mov_b32_e32 v16, v17
	v_mov_b32_e32 v17, v8
	v_pk_fma_f32 v[16:17], v[18:19], v[16:17], v[26:27] op_sel_hi:[0,1,1]
	v_pk_fma_f32 v[16:17], v[12:13], v[8:9], v[16:17] op_sel_hi:[0,1,1]
	v_pk_fma_f32 v[26:27], v[20:21], v[8:9], v[4:5] op_sel_hi:[0,1,0]
	v_pk_mov_b32 v[8:9], v[8:9], v[24:25] op_sel:[1,0]
	s_nop 0
	v_pk_fma_f32 v[8:9], v[18:19], v[8:9], v[26:27] op_sel_hi:[0,1,1]
	v_pk_fma_f32 v[24:25], v[12:13], v[10:11], v[8:9] op_sel_hi:[0,1,1]
	v_pk_fma_f32 v[8:9], v[20:21], v[10:11], v[4:5] op_sel_hi:[0,1,0]
	v_pk_mov_b32 v[10:11], v[10:11], v[14:15] op_sel:[1,0]
	s_nop 0
	v_pk_fma_f32 v[8:9], v[18:19], v[10:11], v[8:9] op_sel_hi:[0,1,1]
	v_pk_fma_f32 v[10:11], v[12:13], v[14:15], v[8:9] op_sel_hi:[0,1,1]
	v_pk_fma_f32 v[8:9], v[20:21], v[14:15], v[4:5] op_sel_hi:[0,1,0]
	v_pk_fma_f32 v[8:9], v[18:19], v[22:23], v[8:9] op_sel_hi:[0,1,1]
	v_mov_b32_e32 v4, v23
	v_pk_fma_f32 v[4:5], v[12:13], v[4:5], v[8:9] op_sel_hi:[0,1,1]
	v_cvt_pk_bf16_f32 v8, v16, v17
	v_cvt_pk_bf16_f32 v9, v24, v25
	v_cvt_pk_bf16_f32 v10, v10, v11
	v_cvt_pk_bf16_f32 v11, v4, v5
	ds_write_b128 v3, v[8:11] offset:20480

.LBB0_667:
	s_setprio 0
	s_mov_b64 s[4:5], 0

.LBB0_683:
	s_and_b32 s39, s11, 3
	v_and_b32_e32 v9, 15, v8
	v_and_b32_e32 v142, 48, v8
	v_lshlrev_b32_e32 v8, 2, v8
	v_lshl_add_u64 v[10:11], s[6:7], 0, v[130:131]
	v_mov_b32_e32 v135, v131
	v_lshl_or_b32 v143, s12, 6, v9
	v_lshl_or_b32 v9, v9, 6, v142
	v_and_b32_e32 v8, 32, v8
	s_lshl_b32 s11, s12, 13
	s_lshl_b32 s12, s39, 12
	v_lshl_add_u64 v[12:13], s[6:7], 0, v[134:135]
	v_mov_b32_e32 v133, v131
	v_bitop3_b32 v18, v9, s11, v8 bitop3:0xde
	v_bitop3_b32 v144, v9, s12, v8 bitop3:0xde
	s_add_i32 m0, s18, 0x18000
	v_lshl_add_u64 v[8:9], v[10:11], 0, s[30:31]
	v_lshl_add_u64 v[14:15], s[4:5], 0, v[132:133]
	v_mov_b32_e32 v137, v131
	s_waitcnt vmcnt(4)
	s_barrier
	v_cmp_lt_u32_e32 vcc, 0xff, v0
	s_nop 3
	s_cbranch_vccz .Lmy_spm_fnc
	s_setprio 1
.Lmy_spm_fnc:
	global_load_lds_dwordx4 v[8:9], off
	v_lshl_add_u64 v[8:9], v[12:13], 0, s[30:31]
	s_add_i32 m0, s18, 0x1a000
	s_add_i32 s42, s18, 0x8000
	s_add_i32 s64, s18, 0xa000
	v_lshl_add_u64 v[16:17], s[4:5], 0, v[136:137]
	global_load_lds_dwordx4 v[8:9], off
	v_lshl_add_u64 v[8:9], v[14:15], 0, s[30:31]
	s_mov_b32 m0, s42
	s_add_u32 s12, s6, 0x8080
	global_load_lds_dwordx4 v[8:9], off
	v_lshl_add_u64 v[8:9], v[16:17], 0, s[30:31]
	s_mov_b32 m0, s64
	s_addc_u32 s13, s7, 0
	global_load_lds_dwordx4 v[8:9], off
	s_add_i32 m0, s18, 0x1c000
	v_lshl_add_u64 v[8:9], s[12:13], 0, v[130:131]
	global_load_lds_dwordx4 v[8:9], off
	v_lshl_add_u64 v[8:9], s[12:13], 0, v[134:135]
	s_add_i32 m0, s18, 0x1e000
	s_add_u32 s10, s68, s10
	global_load_lds_dwordx4 v[8:9], off
	v_lshlrev_b32_e32 v8, 15, v2
	v_and_b32_e32 v8, 0xffff0000, v8
	v_lshl_add_u32 v4, v4, 12, v8
	v_and_b32_e32 v2, 1, v2
	v_lshl_or_b32 v2, v2, 6, v4
	v_lshl_add_u32 v4, v5, 1, v2
	v_lshlrev_b32_e32 v2, 15, v3
	v_and_b32_e32 v2, 0xffff0000, v2
	v_lshl_add_u32 v2, v6, 12, v2
	v_and_b32_e32 v3, 1, v3
	s_waitcnt vmcnt(6)
	v_lshl_or_b32 v2, v3, 6, v2
	v_mov_b32_e32 v5, v131
	s_addc_u32 s11, s69, 0
	v_lshl_add_u32 v2, v7, 1, v2
	v_mov_b32_e32 v3, v131
	v_mov_b32_e32 v10, 0
	v_lshl_add_u64 v[138:139], s[10:11], 0, v[4:5]
	v_lshl_add_u64 v[140:141], s[10:11], 0, v[2:3]
	s_mov_b32 s84, -2
	s_mov_b64 s[10:11], 0x370a8080
	v_add_u32_e32 v145, 0, v18
	v_mov_b32_e32 v11, v10
	v_mov_b32_e32 v12, v10
	v_mov_b32_e32 v13, v10
	v_mov_b32_e32 v14, v10
	v_mov_b32_e32 v15, v10
	v_mov_b32_e32 v16, v10
	v_mov_b32_e32 v17, v10
	v_mov_b32_e32 v26, v10
	v_mov_b32_e32 v27, v10
	v_mov_b32_e32 v28, v10
	v_mov_b32_e32 v29, v10
	v_mov_b32_e32 v30, v10
	v_mov_b32_e32 v31, v10
	v_mov_b32_e32 v32, v10
	v_mov_b32_e32 v33, v10
	v_mov_b32_e32 v2, v10
	v_mov_b32_e32 v3, v10
	v_mov_b32_e32 v4, v10
	v_mov_b32_e32 v5, v10
	v_mov_b32_e32 v6, v10
	v_mov_b32_e32 v7, v10
	v_mov_b32_e32 v8, v10
	v_mov_b32_e32 v9, v10
	v_mov_b32_e32 v18, v10
	v_mov_b32_e32 v19, v10
	v_mov_b32_e32 v20, v10
	v_mov_b32_e32 v21, v10
	v_mov_b32_e32 v22, v10
	v_mov_b32_e32 v23, v10
	v_mov_b32_e32 v24, v10
	v_mov_b32_e32 v25, v10
	v_mov_b32_e32 v34, v10
	v_mov_b32_e32 v35, v10
	v_mov_b32_e32 v36, v10
	v_mov_b32_e32 v37, v10
	v_mov_b32_e32 v38, v10
	v_mov_b32_e32 v39, v10
	v_mov_b32_e32 v40, v10
	v_mov_b32_e32 v41, v10
	v_mov_b32_e32 v50, v10
	v_mov_b32_e32 v51, v10
	v_mov_b32_e32 v52, v10
	v_mov_b32_e32 v53, v10
	v_mov_b32_e32 v54, v10
	v_mov_b32_e32 v55, v10
	v_mov_b32_e32 v56, v10
	v_mov_b32_e32 v57, v10
	v_mov_b32_e32 v66, v10
	v_mov_b32_e32 v67, v10
	v_mov_b32_e32 v68, v10
	v_mov_b32_e32 v69, v10
	v_mov_b32_e32 v70, v10
	v_mov_b32_e32 v71, v10
	v_mov_b32_e32 v72, v10
	v_mov_b32_e32 v73, v10
	v_mov_b32_e32 v74, v10
	v_mov_b32_e32 v75, v10
	v_mov_b32_e32 v76, v10
	v_mov_b32_e32 v77, v10
	v_mov_b32_e32 v78, v10
	v_mov_b32_e32 v79, v10
	v_mov_b32_e32 v80, v10
	v_mov_b32_e32 v81, v10
	v_mov_b32_e32 v90, v10
	v_mov_b32_e32 v91, v10
	v_mov_b32_e32 v92, v10
	v_mov_b32_e32 v93, v10
	v_mov_b32_e32 v94, v10
	v_mov_b32_e32 v95, v10
	v_mov_b32_e32 v96, v10
	v_mov_b32_e32 v97, v10
	v_mov_b32_e32 v106, v10
	v_mov_b32_e32 v107, v10
	v_mov_b32_e32 v108, v10
	v_mov_b32_e32 v109, v10
	v_mov_b32_e32 v110, v10
	v_mov_b32_e32 v111, v10
	v_mov_b32_e32 v112, v10
	v_mov_b32_e32 v113, v10
	v_mov_b32_e32 v82, v10
	v_mov_b32_e32 v83, v10
	v_mov_b32_e32 v84, v10
	v_mov_b32_e32 v85, v10
	v_mov_b32_e32 v86, v10
	v_mov_b32_e32 v87, v10
	v_mov_b32_e32 v88, v10
	v_mov_b32_e32 v89, v10
	v_mov_b32_e32 v98, v10
	v_mov_b32_e32 v99, v10
	v_mov_b32_e32 v100, v10
	v_mov_b32_e32 v101, v10
	v_mov_b32_e32 v102, v10
	v_mov_b32_e32 v103, v10
	v_mov_b32_e32 v104, v10
	v_mov_b32_e32 v105, v10
	v_mov_b32_e32 v114, v10
	v_mov_b32_e32 v115, v10
	v_mov_b32_e32 v116, v10
	v_mov_b32_e32 v117, v10
	v_mov_b32_e32 v118, v10
	v_mov_b32_e32 v119, v10
	v_mov_b32_e32 v120, v10
	v_mov_b32_e32 v121, v10
	v_mov_b32_e32 v122, v10
	v_mov_b32_e32 v123, v10
	v_mov_b32_e32 v124, v10
	v_mov_b32_e32 v125, v10
	v_mov_b32_e32 v126, v10
	v_mov_b32_e32 v127, v10
	v_mov_b32_e32 v128, v10
	v_mov_b32_e32 v129, v10
	v_mov_b32_e32 v58, v10
	v_mov_b32_e32 v59, v10
	v_mov_b32_e32 v60, v10
	v_mov_b32_e32 v61, v10
	v_mov_b32_e32 v62, v10
	v_mov_b32_e32 v63, v10
	v_mov_b32_e32 v64, v10
	v_mov_b32_e32 v65, v10
	v_mov_b32_e32 v42, v10
	v_mov_b32_e32 v43, v10
	v_mov_b32_e32 v44, v10
	v_mov_b32_e32 v45, v10
	v_mov_b32_e32 v46, v10
	v_mov_b32_e32 v47, v10
	v_mov_b32_e32 v48, v10
	v_mov_b32_e32 v49, v10
	s_barrier
.LBB0_684:
	s_add_u32 s12, s10, 0xc8f58080
	s_addc_u32 s13, s11, -1
	s_cmp_lg_u32 s84, 28
	s_cselect_b32 s12, s12, 0
	s_cselect_b32 s13, s13, 0
	s_add_u32 s14, s4, s12
	s_addc_u32 s15, s5, s13
	s_add_u32 s12, s6, s12
	s_addc_u32 s13, s7, s13
	s_add_i32 s27, 0, 0x10000
	v_add_u32_e32 v158, s27, v144
	ds_read_b128 v[146:149], v158
	ds_read_b128 v[150:153], v158 offset:1024
	ds_read_b128 v[154:157], v158 offset:2048
	ds_read_b128 v[158:161], v158 offset:3072
	v_lshl_add_u64 v[174:175], v[138:139], 0, s[10:11]
	s_add_i32 m0, s18, 0xc000
	ds_read_b128 v[162:165], v145
	ds_read_b128 v[166:169], v145 offset:1024
	ds_read_b128 v[170:173], v145 offset:2048
	ds_read_b128 v[178:181], v145 offset:3072
	ds_read_b128 v[182:185], v145 offset:4096
	ds_read_b128 v[188:191], v145 offset:5120
	ds_read_b128 v[192:195], v145 offset:6144
	ds_read_b128 v[196:199], v145 offset:7168
	global_load_lds_dwordx4 v[174:175], off
	v_lshl_add_u64 v[174:175], v[140:141], 0, s[10:11]
	s_add_i32 m0, s18, 0xe000
	s_nop 0
	global_load_lds_dwordx4 v[174:175], off
	s_waitcnt lgkmcnt(8)
	s_waitcnt vmcnt(10)
	s_barrier
	s_waitcnt lgkmcnt(7)
	v_mfma_f32_16x16x32_bf16 v[126:129], v[146:149], v[162:165], v[126:129]
	s_waitcnt lgkmcnt(5)
	v_mfma_f32_16x16x32_bf16 v[122:125], v[154:157], v[162:165], v[122:125]
	v_mfma_f32_16x16x32_bf16 v[118:121], v[146:149], v[170:173], v[118:121]
	s_waitcnt lgkmcnt(3)
	v_mfma_f32_16x16x32_bf16 v[114:117], v[154:157], v[170:173], v[114:117]
	v_mfma_f32_16x16x32_bf16 v[102:105], v[146:149], v[182:185], v[102:105]
	s_waitcnt lgkmcnt(1)
	v_mfma_f32_16x16x32_bf16 v[98:101], v[154:157], v[182:185], v[98:101]
	v_mfma_f32_16x16x32_bf16 v[86:89], v[146:149], v[192:195], v[86:89]
	v_mfma_f32_16x16x32_bf16 v[82:85], v[154:157], v[192:195], v[82:85]
	v_mfma_f32_16x16x32_bf16 v[126:129], v[150:153], v[166:169], v[126:129]
	v_mfma_f32_16x16x32_bf16 v[122:125], v[158:161], v[166:169], v[122:125]
	v_mfma_f32_16x16x32_bf16 v[118:121], v[150:153], v[178:181], v[118:121]
	v_mfma_f32_16x16x32_bf16 v[114:117], v[158:161], v[178:181], v[114:117]
	v_mfma_f32_16x16x32_bf16 v[102:105], v[150:153], v[188:191], v[102:105]
	s_waitcnt lgkmcnt(0)
	v_mfma_f32_16x16x32_bf16 v[98:101], v[158:161], v[188:191], v[98:101]
	v_mfma_f32_16x16x32_bf16 v[86:89], v[150:153], v[196:199], v[86:89]
	v_mfma_f32_16x16x32_bf16 v[82:85], v[158:161], v[196:199], v[82:85]
	s_barrier
	s_add_i32 s43, 0, 0x14000
	v_add_u32_e32 v174, s43, v144
	s_add_i32 s27, s27, s17
	ds_read_b128 v[218:221], v174
	ds_read_b128 v[222:225], v174 offset:1024
	ds_read_b128 v[226:229], v174 offset:2048
	ds_read_b128 v[230:233], v174 offset:3072
	v_lshl_add_u64 v[174:175], s[12:13], 0, v[130:131]
	s_mov_b32 m0, s27
	v_lshl_add_u64 v[200:201], s[12:13], 0, v[134:135]
	global_load_lds_dwordx4 v[174:175], off
	s_add_i32 m0, s27, 0x2000
	s_nop 0
	global_load_lds_dwordx4 v[200:201], off
	s_waitcnt vmcnt(10)
	s_barrier
	s_waitcnt lgkmcnt(3)
	s_waitcnt lgkmcnt(1)
	v_mfma_f32_16x16x32_bf16 v[110:113], v[218:221], v[162:165], v[110:113]
	v_mfma_f32_16x16x32_bf16 v[106:109], v[226:229], v[162:165], v[106:109]
	v_mfma_f32_16x16x32_bf16 v[94:97], v[218:221], v[170:173], v[94:97]
	v_mfma_f32_16x16x32_bf16 v[90:93], v[226:229], v[170:173], v[90:93]
	v_mfma_f32_16x16x32_bf16 v[78:81], v[218:221], v[182:185], v[78:81]
	v_mfma_f32_16x16x32_bf16 v[74:77], v[226:229], v[182:185], v[74:77]
	v_mfma_f32_16x16x32_bf16 v[70:73], v[218:221], v[192:195], v[70:73]
	v_mfma_f32_16x16x32_bf16 v[66:69], v[226:229], v[192:195], v[66:69]
	s_waitcnt lgkmcnt(0)
	v_mfma_f32_16x16x32_bf16 v[110:113], v[222:225], v[166:169], v[110:113]
	v_mfma_f32_16x16x32_bf16 v[106:109], v[230:233], v[166:169], v[106:109]
	v_mfma_f32_16x16x32_bf16 v[94:97], v[222:225], v[178:181], v[94:97]
	v_mfma_f32_16x16x32_bf16 v[90:93], v[230:233], v[178:181], v[90:93]
	v_mfma_f32_16x16x32_bf16 v[78:81], v[222:225], v[188:191], v[78:81]
	v_mfma_f32_16x16x32_bf16 v[74:77], v[230:233], v[188:191], v[74:77]
	v_mfma_f32_16x16x32_bf16 v[70:73], v[222:225], v[196:199], v[70:73]
	v_mfma_f32_16x16x32_bf16 v[66:69], v[230:233], v[196:199], v[66:69]
	s_mov_b32 m0, s18
	v_lshl_add_u64 v[234:235], s[14:15], 0, v[132:133]
	s_barrier
	ds_read_b128 v[162:165], v145 offset:16384
	ds_read_b128 v[166:169], v145 offset:17408
	ds_read_b128 v[170:173], v145 offset:18432
	ds_read_b128 v[178:181], v145 offset:19456
	ds_read_b128 v[182:185], v145 offset:20480
	ds_read_b128 v[188:191], v145 offset:21504
	ds_read_b128 v[192:195], v145 offset:22528
	ds_read_b128 v[196:199], v145 offset:23552
	global_load_lds_dwordx4 v[234:235], off
	v_lshl_add_u64 v[236:237], s[14:15], 0, v[136:137]
	s_mov_b32 m0, s19
	s_nop 0
	global_load_lds_dwordx4 v[236:237], off
	s_barrier
	s_waitcnt lgkmcnt(7)
	v_mfma_f32_16x16x32_bf16 v[54:57], v[146:149], v[162:165], v[54:57]
	s_waitcnt lgkmcnt(5)
	v_mfma_f32_16x16x32_bf16 v[50:53], v[154:157], v[162:165], v[50:53]
	v_mfma_f32_16x16x32_bf16 v[38:41], v[146:149], v[170:173], v[38:41]
	s_waitcnt lgkmcnt(3)
	v_mfma_f32_16x16x32_bf16 v[34:37], v[154:157], v[170:173], v[34:37]
	v_mfma_f32_16x16x32_bf16 v[22:25], v[146:149], v[182:185], v[22:25]
	s_waitcnt lgkmcnt(1)
	v_mfma_f32_16x16x32_bf16 v[18:21], v[154:157], v[182:185], v[18:21]
	v_mfma_f32_16x16x32_bf16 v[6:9], v[146:149], v[192:195], v[6:9]
	v_mfma_f32_16x16x32_bf16 v[2:5], v[154:157], v[192:195], v[2:5]
	v_mfma_f32_16x16x32_bf16 v[54:57], v[150:153], v[166:169], v[54:57]
	v_mfma_f32_16x16x32_bf16 v[50:53], v[158:161], v[166:169], v[50:53]
	v_mfma_f32_16x16x32_bf16 v[38:41], v[150:153], v[178:181], v[38:41]
	v_mfma_f32_16x16x32_bf16 v[34:37], v[158:161], v[178:181], v[34:37]
	v_mfma_f32_16x16x32_bf16 v[22:25], v[150:153], v[188:191], v[22:25]
	s_waitcnt lgkmcnt(0)
	v_mfma_f32_16x16x32_bf16 v[18:21], v[158:161], v[188:191], v[18:21]
	v_mfma_f32_16x16x32_bf16 v[6:9], v[150:153], v[196:199], v[6:9]
	v_mfma_f32_16x16x32_bf16 v[2:5], v[158:161], v[196:199], v[2:5]
	s_barrier
	s_add_u32 s60, s12, 0x8000
	s_addc_u32 s61, s13, 0
	s_add_i32 s27, s43, s17
	v_lshl_add_u64 v[146:147], s[60:61], 0, v[130:131]
	s_mov_b32 m0, s27
	s_nop 0
	global_load_lds_dwordx4 v[146:147], off
	v_lshl_add_u64 v[146:147], s[60:61], 0, v[134:135]
	s_add_i32 m0, s27, 0x2000
	s_nop 0
	global_load_lds_dwordx4 v[146:147], off
	s_waitcnt vmcnt(10)
	s_barrier
	v_mfma_f32_16x16x32_bf16 v[30:33], v[218:221], v[162:165], v[30:33]
	v_mfma_f32_16x16x32_bf16 v[26:29], v[226:229], v[162:165], v[26:29]
	v_mfma_f32_16x16x32_bf16 v[14:17], v[218:221], v[170:173], v[14:17]
	v_mfma_f32_16x16x32_bf16 v[10:13], v[226:229], v[170:173], v[10:13]
	v_mfma_f32_16x16x32_bf16 v[58:61], v[218:221], v[182:185], v[58:61]
	v_mfma_f32_16x16x32_bf16 v[62:65], v[226:229], v[182:185], v[62:65]
	v_mfma_f32_16x16x32_bf16 v[42:45], v[218:221], v[192:195], v[42:45]
	v_mfma_f32_16x16x32_bf16 v[46:49], v[226:229], v[192:195], v[46:49]
	v_mfma_f32_16x16x32_bf16 v[30:33], v[222:225], v[166:169], v[30:33]
	v_mfma_f32_16x16x32_bf16 v[26:29], v[230:233], v[166:169], v[26:29]
	v_mfma_f32_16x16x32_bf16 v[14:17], v[222:225], v[178:181], v[14:17]
	v_mfma_f32_16x16x32_bf16 v[10:13], v[230:233], v[178:181], v[10:13]
	v_mfma_f32_16x16x32_bf16 v[58:61], v[222:225], v[188:191], v[58:61]
	v_mfma_f32_16x16x32_bf16 v[62:65], v[230:233], v[188:191], v[62:65]
	v_mfma_f32_16x16x32_bf16 v[42:45], v[222:225], v[196:199], v[42:45]
	v_mfma_f32_16x16x32_bf16 v[46:49], v[230:233], v[196:199], v[46:49]
	s_add_i32 s27, 0, 0x18000
	v_add_u32_e32 v158, s27, v144
	s_barrier
	ds_read_b128 v[146:149], v158
	ds_read_b128 v[150:153], v158 offset:1024
	ds_read_b128 v[154:157], v158 offset:2048
	ds_read_b128 v[158:161], v158 offset:3072
	s_add_u32 s14, s14, 0x80000
	s_addc_u32 s15, s15, 0
	s_mov_b32 m0, s33
	v_lshl_add_u64 v[218:219], s[14:15], 0, v[132:133]
	ds_read_b128 v[162:165], v145 offset:32768
	ds_read_b128 v[166:169], v145 offset:33792
	ds_read_b128 v[170:173], v145 offset:34816
	ds_read_b128 v[178:181], v145 offset:35840
	ds_read_b128 v[182:185], v145 offset:36864
	ds_read_b128 v[188:191], v145 offset:37888
	ds_read_b128 v[192:195], v145 offset:38912
	ds_read_b128 v[196:199], v145 offset:39936
	global_load_lds_dwordx4 v[218:219], off
	v_lshl_add_u64 v[218:219], s[14:15], 0, v[136:137]
	s_mov_b32 m0, s38
	s_nop 0
	global_load_lds_dwordx4 v[218:219], off
	s_waitcnt lgkmcnt(8)
	s_waitcnt vmcnt(10)
	s_barrier
	s_waitcnt lgkmcnt(7)
	v_mfma_f32_16x16x32_bf16 v[126:129], v[146:149], v[162:165], v[126:129]
	s_waitcnt lgkmcnt(5)
	v_mfma_f32_16x16x32_bf16 v[122:125], v[154:157], v[162:165], v[122:125]
	v_mfma_f32_16x16x32_bf16 v[118:121], v[146:149], v[170:173], v[118:121]
	s_waitcnt lgkmcnt(3)
	v_mfma_f32_16x16x32_bf16 v[114:117], v[154:157], v[170:173], v[114:117]
	v_mfma_f32_16x16x32_bf16 v[102:105], v[146:149], v[182:185], v[102:105]
	s_waitcnt lgkmcnt(1)
	v_mfma_f32_16x16x32_bf16 v[98:101], v[154:157], v[182:185], v[98:101]
	v_mfma_f32_16x16x32_bf16 v[86:89], v[146:149], v[192:195], v[86:89]
	v_mfma_f32_16x16x32_bf16 v[82:85], v[154:157], v[192:195], v[82:85]
	v_mfma_f32_16x16x32_bf16 v[126:129], v[150:153], v[166:169], v[126:129]
	v_mfma_f32_16x16x32_bf16 v[122:125], v[158:161], v[166:169], v[122:125]
	v_mfma_f32_16x16x32_bf16 v[118:121], v[150:153], v[178:181], v[118:121]
	v_mfma_f32_16x16x32_bf16 v[114:117], v[158:161], v[178:181], v[114:117]
	v_mfma_f32_16x16x32_bf16 v[102:105], v[150:153], v[188:191], v[102:105]
	s_waitcnt lgkmcnt(0)
	v_mfma_f32_16x16x32_bf16 v[98:101], v[158:161], v[188:191], v[98:101]
	v_mfma_f32_16x16x32_bf16 v[86:89], v[150:153], v[196:199], v[86:89]
	v_mfma_f32_16x16x32_bf16 v[82:85], v[158:161], v[196:199], v[82:85]
	s_barrier
	s_add_i32 s14, 0, 0x1c000
	s_add_i32 s15, s27, s17
	v_add_u32_e32 v187, s14, v144
	v_lshl_add_u64 v[174:175], v[174:175], 0, s[30:31]
	s_mov_b32 m0, s15
	ds_read_b128 v[218:221], v187
	ds_read_b128 v[222:225], v187 offset:1024
	ds_read_b128 v[226:229], v187 offset:2048
	ds_read_b128 v[230:233], v187 offset:3072
	global_load_lds_dwordx4 v[174:175], off
	v_lshl_add_u64 v[174:175], v[200:201], 0, s[30:31]
	s_add_i32 m0, s15, 0x2000
	s_nop 0
	global_load_lds_dwordx4 v[174:175], off
	s_waitcnt vmcnt(10)
	s_barrier
	s_waitcnt lgkmcnt(3)
	s_waitcnt lgkmcnt(1)
	v_mfma_f32_16x16x32_bf16 v[110:113], v[218:221], v[162:165], v[110:113]
	v_mfma_f32_16x16x32_bf16 v[106:109], v[226:229], v[162:165], v[106:109]
	v_mfma_f32_16x16x32_bf16 v[94:97], v[218:221], v[170:173], v[94:97]
	v_mfma_f32_16x16x32_bf16 v[90:93], v[226:229], v[170:173], v[90:93]
	v_mfma_f32_16x16x32_bf16 v[78:81], v[218:221], v[182:185], v[78:81]
	v_mfma_f32_16x16x32_bf16 v[74:77], v[226:229], v[182:185], v[74:77]
	v_mfma_f32_16x16x32_bf16 v[70:73], v[218:221], v[192:195], v[70:73]
	v_mfma_f32_16x16x32_bf16 v[66:69], v[226:229], v[192:195], v[66:69]
	s_waitcnt lgkmcnt(0)
	v_mfma_f32_16x16x32_bf16 v[110:113], v[222:225], v[166:169], v[110:113]
	v_mfma_f32_16x16x32_bf16 v[106:109], v[230:233], v[166:169], v[106:109]
	v_mfma_f32_16x16x32_bf16 v[94:97], v[222:225], v[178:181], v[94:97]
	v_mfma_f32_16x16x32_bf16 v[90:93], v[230:233], v[178:181], v[90:93]
	v_mfma_f32_16x16x32_bf16 v[78:81], v[222:225], v[188:191], v[78:81]
	v_mfma_f32_16x16x32_bf16 v[74:77], v[230:233], v[188:191], v[74:77]
	v_mfma_f32_16x16x32_bf16 v[70:73], v[222:225], v[196:199], v[70:73]
	v_mfma_f32_16x16x32_bf16 v[66:69], v[230:233], v[196:199], v[66:69]
	s_mov_b32 m0, s42
	v_lshl_add_u64 v[174:175], v[234:235], 0, s[30:31]
	s_barrier
	ds_read_b128 v[162:165], v145 offset:49152
	ds_read_b128 v[166:169], v145 offset:50176
	ds_read_b128 v[170:173], v145 offset:51200
	ds_read_b128 v[178:181], v145 offset:52224
	ds_read_b128 v[182:185], v145 offset:53248
	ds_read_b128 v[188:191], v145 offset:54272
	ds_read_b128 v[192:195], v145 offset:55296
	ds_read_b128 v[196:199], v145 offset:56320
	global_load_lds_dwordx4 v[174:175], off
	v_lshl_add_u64 v[174:175], v[236:237], 0, s[30:31]
	s_mov_b32 m0, s64
	s_nop 0
	global_load_lds_dwordx4 v[174:175], off
	s_barrier
	s_waitcnt lgkmcnt(7)
	v_mfma_f32_16x16x32_bf16 v[54:57], v[146:149], v[162:165], v[54:57]
	s_waitcnt lgkmcnt(5)
	v_mfma_f32_16x16x32_bf16 v[50:53], v[154:157], v[162:165], v[50:53]
	v_mfma_f32_16x16x32_bf16 v[38:41], v[146:149], v[170:173], v[38:41]
	s_waitcnt lgkmcnt(3)
	v_mfma_f32_16x16x32_bf16 v[34:37], v[154:157], v[170:173], v[34:37]
	v_mfma_f32_16x16x32_bf16 v[22:25], v[146:149], v[182:185], v[22:25]
	s_waitcnt lgkmcnt(1)
	v_mfma_f32_16x16x32_bf16 v[18:21], v[154:157], v[182:185], v[18:21]
	v_mfma_f32_16x16x32_bf16 v[6:9], v[146:149], v[192:195], v[6:9]
	v_mfma_f32_16x16x32_bf16 v[2:5], v[154:157], v[192:195], v[2:5]
	v_mfma_f32_16x16x32_bf16 v[54:57], v[150:153], v[166:169], v[54:57]
	v_mfma_f32_16x16x32_bf16 v[50:53], v[158:161], v[166:169], v[50:53]
	v_mfma_f32_16x16x32_bf16 v[38:41], v[150:153], v[178:181], v[38:41]
	v_mfma_f32_16x16x32_bf16 v[34:37], v[158:161], v[178:181], v[34:37]
	v_mfma_f32_16x16x32_bf16 v[22:25], v[150:153], v[188:191], v[22:25]
	s_waitcnt lgkmcnt(0)
	v_mfma_f32_16x16x32_bf16 v[18:21], v[158:161], v[188:191], v[18:21]
	v_mfma_f32_16x16x32_bf16 v[6:9], v[150:153], v[196:199], v[6:9]
	v_mfma_f32_16x16x32_bf16 v[2:5], v[158:161], v[196:199], v[2:5]
	s_barrier
	s_add_u32 s12, s12, 0x8080
	s_addc_u32 s13, s13, 0
	s_add_i32 s14, s14, s17
	v_lshl_add_u64 v[146:147], s[12:13], 0, v[130:131]
	s_mov_b32 m0, s14
	s_nop 0
	global_load_lds_dwordx4 v[146:147], off
	v_lshl_add_u64 v[146:147], s[12:13], 0, v[134:135]
	s_add_i32 m0, s14, 0x2000
	s_nop 0
	global_load_lds_dwordx4 v[146:147], off
	s_waitcnt vmcnt(10)
	s_barrier
	v_mfma_f32_16x16x32_bf16 v[30:33], v[218:221], v[162:165], v[30:33]
	v_mfma_f32_16x16x32_bf16 v[26:29], v[226:229], v[162:165], v[26:29]
	v_mfma_f32_16x16x32_bf16 v[14:17], v[218:221], v[170:173], v[14:17]
	v_mfma_f32_16x16x32_bf16 v[10:13], v[226:229], v[170:173], v[10:13]
	v_mfma_f32_16x16x32_bf16 v[58:61], v[218:221], v[182:185], v[58:61]
	v_mfma_f32_16x16x32_bf16 v[62:65], v[226:229], v[182:185], v[62:65]
	v_mfma_f32_16x16x32_bf16 v[42:45], v[218:221], v[192:195], v[42:45]
	v_mfma_f32_16x16x32_bf16 v[46:49], v[226:229], v[192:195], v[46:49]
	v_mfma_f32_16x16x32_bf16 v[30:33], v[222:225], v[166:169], v[30:33]
	v_mfma_f32_16x16x32_bf16 v[26:29], v[230:233], v[166:169], v[26:29]
	v_mfma_f32_16x16x32_bf16 v[14:17], v[222:225], v[178:181], v[14:17]
	v_mfma_f32_16x16x32_bf16 v[10:13], v[230:233], v[178:181], v[10:13]
	v_mfma_f32_16x16x32_bf16 v[58:61], v[222:225], v[188:191], v[58:61]
	v_mfma_f32_16x16x32_bf16 v[62:65], v[230:233], v[188:191], v[62:65]
	v_mfma_f32_16x16x32_bf16 v[42:45], v[222:225], v[196:199], v[42:45]
	v_mfma_f32_16x16x32_bf16 v[46:49], v[230:233], v[196:199], v[46:49]
	s_add_i32 s84, s84, 2
	s_add_u32 s10, s10, 0x100
	s_addc_u32 s11, s11, 0
	s_cmp_gt_u32 s84, 29
	s_barrier
	s_cbranch_scc0 .LBB0_684
	s_mul_i32 s4, s22, 0x900
	s_lshl_b32 s5, s16, 8
	s_add_i32 s22, s4, s5
	s_lshl_b32 s6, s39, 6
	s_lshl_b64 s[4:5], s[22:23], 11
	s_add_u32 s4, s68, s4
	v_lshlrev_b32_e32 v130, 10, v143
	s_addc_u32 s5, s69, s5
	v_or3_b32 v130, v130, s6, v142
	v_cvt_pk_bf16_f32 v126, v126, v127
	v_lshl_add_u64 v[132:133], v[130:131], 1, s[4:5]
	s_mov_b64 s[4:5], 0x5ed68600
	v_lshl_add_u64 v[134:135], v[132:133], 0, s[4:5]
	s_mov_b32 s4, 0x5ed68000
	v_cvt_pk_bf16_f32 v127, v128, v129
	v_cvt_pk_bf16_f32 v128, v122, v123
	v_add_co_u32_e32 v122, vcc, s4, v132
	v_cvt_pk_bf16_f32 v110, v110, v111
	s_nop 0
	v_addc_co_u32_e32 v123, vcc, 0, v133, vcc
	v_cvt_pk_bf16_f32 v111, v112, v113
	v_cvt_pk_bf16_f32 v112, v106, v107
	v_cvt_pk_bf16_f32 v113, v108, v109
	s_mov_b32 s4, 0x5ed70000
	global_store_dwordx4 v[134:135], v[110:113], off offset:16
	v_cvt_pk_bf16_f32 v94, v94, v95
	v_cvt_pk_bf16_f32 v95, v96, v97
	v_add_co_u32_e32 v110, vcc, s4, v132
	v_cvt_pk_bf16_f32 v96, v90, v91
	s_nop 0
	v_addc_co_u32_e32 v111, vcc, 0, v133, vcc
	v_cvt_pk_bf16_f32 v97, v92, v93
	s_mov_b32 s4, 0x5ed78000
	global_store_dwordx4 v[110:111], v[94:97], off offset:1552
	v_cvt_pk_bf16_f32 v78, v78, v79
	v_cvt_pk_bf16_f32 v79, v80, v81
	v_add_co_u32_e32 v94, vcc, s4, v132
	v_cvt_pk_bf16_f32 v80, v74, v75
	s_nop 0
	v_addc_co_u32_e32 v95, vcc, 0, v133, vcc
	v_cvt_pk_bf16_f32 v81, v76, v77
	s_mov_b32 s4, 0x5ed80000
	global_store_dwordx4 v[94:95], v[78:81], off offset:1552
	v_cvt_pk_bf16_f32 v54, v54, v55
	v_cvt_pk_bf16_f32 v55, v56, v57
	v_add_co_u32_e32 v78, vcc, s4, v132
	s_mov_b32 s4, 0x5eda8000
	s_nop 0
	v_addc_co_u32_e32 v79, vcc, 0, v133, vcc
	v_cvt_pk_bf16_f32 v56, v50, v51
	v_add_co_u32_e32 v50, vcc, s4, v132
	v_cvt_pk_bf16_f32 v30, v30, v31
	s_nop 0
	v_addc_co_u32_e32 v51, vcc, 0, v133, vcc
	v_cvt_pk_bf16_f32 v31, v32, v33
	v_cvt_pk_bf16_f32 v32, v26, v27
	v_cvt_pk_bf16_f32 v33, v28, v29
	s_mov_b32 s4, 0x5edb0000
	global_store_dwordx4 v[50:51], v[30:33], off offset:1552
	v_cvt_pk_bf16_f32 v14, v14, v15
	v_cvt_pk_bf16_f32 v15, v16, v17
	v_add_co_u32_e32 v30, vcc, s4, v132
	v_cvt_pk_bf16_f32 v16, v10, v11
	s_nop 0
	v_addc_co_u32_e32 v31, vcc, 0, v133, vcc
	v_cvt_pk_bf16_f32 v17, v12, v13
	s_mov_b32 s4, 0x5edb8000
	global_store_dwordx4 v[30:31], v[14:17], off offset:1552
	v_cvt_pk_bf16_f32 v10, v22, v23
	v_cvt_pk_bf16_f32 v11, v24, v25
	v_add_co_u32_e32 v14, vcc, s4, v132
	v_cvt_pk_bf16_f32 v12, v18, v19
	v_cvt_pk_bf16_f32 v13, v20, v21
	v_addc_co_u32_e32 v15, vcc, 0, v133, vcc
	global_store_dwordx4 v[14:15], v[10:13], off offset:1536
	s_mov_b32 s4, 0x5edc0000
	v_cvt_pk_bf16_f32 v129, v124, v125
	v_cvt_pk_bf16_f32 v10, v58, v59
	v_cvt_pk_bf16_f32 v11, v60, v61
	v_cvt_pk_bf16_f32 v12, v62, v63
	v_cvt_pk_bf16_f32 v13, v64, v65
	global_store_dwordx4 v[14:15], v[10:13], off offset:1552
	v_cvt_pk_bf16_f32 v106, v118, v119
	v_cvt_pk_bf16_f32 v107, v120, v121
	v_add_co_u32_e32 v10, vcc, s4, v132
	v_cvt_pk_bf16_f32 v108, v114, v115
	v_cvt_pk_bf16_f32 v109, v116, v117
	v_cvt_pk_bf16_f32 v90, v102, v103
	v_cvt_pk_bf16_f32 v91, v104, v105
	v_cvt_pk_bf16_f32 v92, v98, v99
	v_cvt_pk_bf16_f32 v93, v100, v101
	v_cvt_pk_bf16_f32 v74, v86, v87
	v_cvt_pk_bf16_f32 v75, v88, v89
	v_cvt_pk_bf16_f32 v76, v82, v83
	v_cvt_pk_bf16_f32 v77, v84, v85
	v_cvt_pk_bf16_f32 v70, v70, v71
	v_cvt_pk_bf16_f32 v71, v72, v73
	v_cvt_pk_bf16_f32 v72, v66, v67
	v_cvt_pk_bf16_f32 v73, v68, v69
	v_cvt_pk_bf16_f32 v57, v52, v53
	v_cvt_pk_bf16_f32 v26, v38, v39
	v_cvt_pk_bf16_f32 v27, v40, v41
	v_cvt_pk_bf16_f32 v28, v34, v35
	v_cvt_pk_bf16_f32 v29, v36, v37
	v_cvt_pk_bf16_f32 v6, v6, v7
	v_cvt_pk_bf16_f32 v7, v8, v9
	v_cvt_pk_bf16_f32 v8, v2, v3
	v_cvt_pk_bf16_f32 v9, v4, v5
	v_addc_co_u32_e32 v11, vcc, 0, v133, vcc
	v_cvt_pk_bf16_f32 v2, v42, v43
	v_cvt_pk_bf16_f32 v3, v44, v45
	v_cvt_pk_bf16_f32 v4, v46, v47
	v_cvt_pk_bf16_f32 v5, v48, v49
	global_store_dwordx4 v[122:123], v[126:129], off offset:1536
	global_store_dwordx4 v[110:111], v[106:109], off offset:1536
	global_store_dwordx4 v[94:95], v[90:93], off offset:1536
	global_store_dwordx4 v[78:79], v[74:77], off offset:1536
	global_store_dwordx4 v[78:79], v[70:73], off offset:1552
	global_store_dwordx4 v[50:51], v[54:57], off offset:1536
	global_store_dwordx4 v[30:31], v[26:29], off offset:1536
	global_store_dwordx4 v[10:11], v[6:9], off offset:1536
	global_store_dwordx4 v[10:11], v[2:5], off offset:1552
	s_waitcnt vmcnt(0)
	s_setprio 0
	s_cmpk_lt_u32 s1, 0x100
	s_cbranch_scc0 .LBB0_687
	s_barrier

.LBB0_698:
	s_andn2_b64 vcc, exec, s[4:5]
	s_cbranch_vccnz .LBB0_789
	v_mov_b32_e32 v136, v0
	s_load_dwordx4 s[4:7], s[66:67], 0x58
	s_lshl_b32 s1, s57, 1
	s_add_i32 s84, s44, s1
	v_readlane_b32 s1, v254, 10
	s_mov_b32 s85, s23
	s_waitcnt lgkmcnt(0)
	s_add_u32 s1, s4, s1
	v_readlane_b32 s4, v254, 12
	s_addc_u32 s4, s5, s4
	v_readlane_b32 s5, v254, 5
	s_add_u32 s5, s6, s5
	v_readlane_b32 s6, v254, 14
	s_addc_u32 s6, s7, s6
	s_lshl_b64 s[90:91], s[84:85], 2
	s_add_u32 s86, s1, s90
	v_lshlrev_b32_e32 v2, 11, v136
	v_add_u32_e32 v31, 0x200, v136
	s_addc_u32 s87, s4, s91
	v_and_b32_e32 v53, 0x7800, v2
	v_ashrrev_i32_e32 v2, 1, v31
	v_add_u32_e32 v138, 0x400, v136
	s_add_u32 s88, s5, s90
	v_and_b32_e32 v2, -8, v2
	s_movk_i32 s1, 0xe00
	v_ashrrev_i32_e32 v4, 1, v138
	s_addc_u32 s89, s6, s91
	s_lshl_b64 s[4:5], s[84:85], 16
	v_add_u32_e32 v2, v2, v53
	v_cmp_gt_i32_e64 s[14:15], s1, v136
	v_and_b32_e32 v4, -8, v4
	s_movk_i32 s1, 0xc00
	s_add_u32 s92, s58, s4
	v_cndmask_b32_e64 v2, 8, v2, s[14:15]
	v_add_u32_e32 v4, v4, v53
	v_cmp_gt_i32_e64 s[12:13], s1, v136
	s_addc_u32 s93, s59, s5
	v_ashrrev_i32_e32 v3, 31, v2
	v_cndmask_b32_e64 v4, 8, v4, s[12:13]
	v_lshl_add_u64 v[2:3], v[2:3], 1, s[92:93]
	v_ashrrev_i32_e32 v5, 31, v4
	v_add_u32_e32 v140, 0x600, v136
	s_waitcnt vmcnt(0)
	s_barrier
	v_readfirstlane_b32 s60, v0
	s_nop 3
	s_cmp_lt_u32 s60, 0x100
	s_cbranch_scc1 .Lmy_spm_hp
	s_setprio 1
.Lmy_spm_hp:
	global_load_dword v30, v1, s[86:87] offset:2048
	global_load_dword v34, v131, s[86:87]
	global_load_dword v32, v131, s[86:87] offset:3072
	global_load_dword v36, v131, s[88:89]
	v_lshl_add_u64 v[4:5], v[4:5], 1, s[92:93]
	global_load_dwordx4 v[26:29], v[2:3], off
	global_load_ushort v51, v[2:3], off offset:16
	global_load_ushort v49, v[4:5], off offset:-2
	global_load_ushort v52, v[2:3], off offset:-2
	v_ashrrev_i32_e32 v2, 1, v140
	v_and_b32_e32 v2, -8, v2
	s_movk_i32 s1, 0xa00
	v_add_u32_e32 v2, v2, v53
	v_cmp_gt_i32_e32 vcc, s1, v136
	v_add_u32_e32 v42, 0x800, v136
	s_movk_i32 s1, 0x800
	v_cndmask_b32_e32 v2, 8, v2, vcc
	v_ashrrev_i32_e32 v3, 31, v2
	v_lshl_add_u64 v[2:3], v[2:3], 1, s[92:93]
	global_load_dwordx4 v[22:25], v[4:5], off
	global_load_ushort v50, v[4:5], off offset:16
	global_load_ushort v47, v[2:3], off offset:-2
	v_ashrrev_i32_e32 v4, 1, v42
	v_and_b32_e32 v4, -8, v4
	v_add_u32_e32 v4, v4, v53
	v_cmp_gt_i32_e64 s[4:5], s1, v136
	v_add_u32_e32 v39, 0xa00, v136
	s_movk_i32 s1, 0x600
	v_cndmask_b32_e64 v4, 8, v4, s[4:5]
	v_ashrrev_i32_e32 v5, 31, v4
	v_lshl_add_u64 v[4:5], v[4:5], 1, s[92:93]
	global_load_dwordx4 v[18:21], v[2:3], off
	global_load_ushort v48, v[2:3], off offset:16
	global_load_ushort v45, v[4:5], off offset:-2
	v_ashrrev_i32_e32 v2, 1, v39
	v_and_b32_e32 v2, -8, v2
	v_add_u32_e32 v2, v2, v53
	v_cmp_gt_i32_e64 s[6:7], s1, v136
	v_add_u32_e32 v35, 0xc00, v136
	s_movk_i32 s1, 0x400
	v_cndmask_b32_e64 v2, 8, v2, s[6:7]
	v_ashrrev_i32_e32 v3, 31, v2
	v_lshl_add_u64 v[2:3], v[2:3], 1, s[92:93]
	global_load_dwordx4 v[14:17], v[4:5], off
	global_load_ushort v46, v[4:5], off offset:16
	global_load_ushort v43, v[2:3], off offset:-2
	v_ashrrev_i32_e32 v4, 1, v35
	v_and_b32_e32 v4, -8, v4
	v_add_u32_e32 v4, v4, v53
	v_cmp_gt_i32_e64 s[8:9], s1, v136
	v_add_u32_e32 v33, 0xe00, v136
	s_movk_i32 s1, 0x200
	v_cndmask_b32_e64 v4, 8, v4, s[8:9]
	v_ashrrev_i32_e32 v5, 31, v4
	v_lshl_add_u64 v[4:5], v[4:5], 1, s[92:93]
	global_load_dwordx4 v[10:13], v[2:3], off
	global_load_ushort v44, v[2:3], off offset:16
	global_load_ushort v40, v[4:5], off offset:-2
	v_ashrrev_i32_e32 v2, 1, v33
	v_and_b32_e32 v2, -8, v2
	v_add_u32_e32 v2, v2, v53
	v_cmp_gt_i32_e64 s[10:11], s1, v136
	v_cmp_gt_i32_e64 s[16:17], s28, v136
	s_nop 0
	v_cndmask_b32_e64 v2, 8, v2, s[10:11]
	v_ashrrev_i32_e32 v3, 31, v2
	v_lshl_add_u64 v[54:55], v[2:3], 1, s[92:93]
	global_load_dwordx4 v[6:9], v[4:5], off
	global_load_ushort v41, v[4:5], off offset:16
	global_load_ushort v38, v[54:55], off offset:-2
	s_nop 0
	global_load_dwordx4 v[2:5], v[54:55], off
	global_load_ushort v37, v[54:55], off offset:16
	s_and_saveexec_b64 s[18:19], s[16:17]
	s_cbranch_execz .LBB0_707
	v_ashrrev_i32_e32 v54, 1, v136
	v_and_b32_e32 v54, -8, v54
	v_add_u32_e32 v54, v54, v53
	v_ashrrev_i32_e32 v55, 31, v54
	v_lshl_add_u64 v[58:59], v[54:55], 1, s[92:93]
	global_load_dwordx4 v[54:57], v[58:59], off
	global_load_ushort v53, v[58:59], off offset:-2
	v_cmp_lt_i32_e64 s[16:17], 15, v136
	s_movk_i32 s1, 0xfef
	s_waitcnt vmcnt(1)
	v_lshlrev_b32_e32 v61, 16, v54
	s_waitcnt vmcnt(0)
	v_lshlrev_b32_e32 v53, 16, v53
	v_cndmask_b32_e64 v60, 0, 1.0, s[16:17]
	v_mul_f32_e32 v60, v60, v53
	global_load_ushort v53, v[58:59], off offset:16
	v_and_b32_e32 v54, 0xffff0000, v54
	v_pk_fma_f32 v[68:69], v[34:35], v[60:61], v[36:37] op_sel_hi:[0,1,0]
	v_mov_b32_e32 v60, v61
	v_mov_b32_e32 v61, v54
	v_and_b32_e32 v67, 16, v56
	v_and_b32_e32 v66, 0xffff0000, v55
	v_lshlrev_b32_e32 v55, 16, v55
	v_pk_fma_f32 v[60:61], v[32:33], v[60:61], v[68:69] op_sel_hi:[0,1,1]
	v_lshlrev_b32_e32 v64, 16, v57
	v_pk_fma_f32 v[60:61], v[30:31], v[54:55], v[60:61] op_sel_hi:[0,1,1]
	v_pk_fma_f32 v[68:69], v[34:35], v[54:55], v[36:37] op_sel_hi:[0,1,0]
	v_pk_mov_b32 v[54:55], v[54:55], v[66:67] op_sel:[1,0]
	v_and_b32_e32 v62, 0xffff0000, v56
	v_and_b32_e32 v65, 0xffff0000, v57
	v_mov_b32_e32 v63, v64
	v_lshlrev_b32_e32 v57, 16, v56
	v_mov_b32_e32 v56, v66
	v_pk_fma_f32 v[54:55], v[32:33], v[54:55], v[68:69] op_sel_hi:[0,1,1]
	v_pk_fma_f32 v[66:67], v[30:31], v[56:57], v[54:55] op_sel_hi:[0,1,1]
	v_pk_fma_f32 v[54:55], v[34:35], v[56:57], v[36:37] op_sel_hi:[0,1,0]
	v_pk_mov_b32 v[56:57], v[56:57], v[62:63] op_sel:[1,0]
	v_cmp_lt_i32_e64 s[16:17], s1, v136
	v_pk_fma_f32 v[54:55], v[32:33], v[56:57], v[54:55] op_sel_hi:[0,1,1]
	v_pk_fma_f32 v[56:57], v[30:31], v[62:63], v[54:55] op_sel_hi:[0,1,1]
	v_cndmask_b32_e64 v58, 1.0, 0, s[16:17]
	v_pk_fma_f32 v[54:55], v[34:35], v[62:63], v[36:37] op_sel_hi:[0,1,0]
	v_pk_fma_f32 v[54:55], v[32:33], v[64:65], v[54:55] op_sel_hi:[0,1,1]
	v_cvt_pk_bf16_f32 v56, v56, v57
	s_waitcnt vmcnt(0)
	v_lshlrev_b32_e32 v53, 16, v53
	v_mul_f32_e32 v59, v58, v53
	v_mov_b32_e32 v58, v65
	v_pk_fma_f32 v[58:59], v[30:31], v[58:59], v[54:55] op_sel_hi:[0,1,1]
	v_cvt_pk_bf16_f32 v54, v60, v61
	v_cvt_pk_bf16_f32 v55, v66, v67
	v_cvt_pk_bf16_f32 v57, v58, v59
	v_lshl_add_u32 v53, v136, 4, 0
	ds_write_b128 v53, v[54:57] offset:20480
	s_or_b64 exec, exec, s[18:19]
	s_and_saveexec_b64 s[16:17], s[14:15]
	s_cbranch_execnz .LBB0_708
